# v52 + loader prologue: priming windows -1,0,1,2 requested per row group back to back (1.5 KB contiguous bursts)
# speedup vs baseline: 1.0042x; 1.0042x over previous
.LBB1_248:
	v_and_b32_e32 v6, 31, v0
	v_bfe_u32 v7, v0, 5, 3
	s_cmp_lt_u32 s8, 0x2000
	s_cselect_b32 s50, s12, s14
	s_cselect_b32 s51, s13, s15
	s_and_b32 s0, s8, 0x1fff
	s_mul_i32 s1, s0, 0x2ee0
	s_add_u32 s50, s50, s1
	s_addc_u32 s51, s51, 0
	s_mov_b32 s52, s50
	s_mov_b32 s53, s51
	s_add_u32 s54, s50, 0x17700
	s_addc_u32 s55, s51, 0
	s_add_u32 s56, s50, 0x2ee00
	s_addc_u32 s57, s51, 0
	s_add_u32 s58, s50, 0x46500
	s_addc_u32 s59, s51, 0
	s_add_u32 s60, s50, 0x5dc00
	s_addc_u32 s61, s51, 0
	s_add_u32 s62, s50, 0x75300
	s_addc_u32 s63, s51, 0
	s_add_u32 s64, s50, 0x8ca00
	s_addc_u32 s65, s51, 0
	s_add_u32 s66, s50, 0xa4100
	s_addc_u32 s67, s51, 0
	v_and_b32_e32 v136, 3, v7
	v_lshl_add_u32 v137, v136, 1, v6
	s_movk_i32 s0, 0x2ee0
	v_mul_lo_u32 v2, v7, s0
	v_lshl_add_u32 v2, v137, 4, v2
	s_movk_i32 s0, 0x110
	v_mul_lo_u32 v3, v7, s0
	v_lshl_add_u32 v138, v137, 3, v3
	v_cmp_le_u32_e64 s[76:77], 32, v137
	v_cmp_gt_u32_e64 s[68:69], 14, v137
	s_not_b64 s[78:79], s[76:77]
	v_mov_b32_e32 v139, 0x0
	v_mov_b32_e32 v140, 0x4300
	v_cndmask_b32_e64 v139, v139, v140, s[76:77]
	v_add_u32_e32 v141, v138, v139
	v_mov_b32_e32 v139, 0x4400
	v_mov_b32_e32 v140, 0x8700
	v_cndmask_b32_e64 v139, v139, v140, s[76:77]
	v_add_u32_e32 v142, v138, v139
	v_mov_b32_e32 v139, 0x8800
	v_mov_b32_e32 v140, 0xcb00
	v_cndmask_b32_e64 v139, v139, v140, s[76:77]
	v_add_u32_e32 v143, v138, v139
	v_mov_b32_e32 v139, 0xcc00
	v_mov_b32_e32 v140, 0xffffff00
	v_cndmask_b32_e64 v139, v139, v140, s[76:77]
	v_add_u32_e32 v144, v138, v139
	s_add_u32 s48, s18, 0x100000
	s_addc_u32 s49, s19, 0
	s_lshl_b32 s0, s10, 12
	v_add_u32_e32 v150, 0xfffffe00, v0
	v_lshl_add_u32 v150, v150, 4, s0
	global_load_dwordx4 v[152:155], v150, s[48:49]
	global_load_dwordx4 v[156:159], v150, s[18:19]
	v_mov_b32_e32 v104, 0
	v_mov_b32_e32 v105, 0
	v_mov_b32_e32 v106, 0
	v_mov_b32_e32 v107, 0
	s_mov_b64 s[70:71], exec
	s_mov_b64 exec, s[76:77]
	global_load_dwordx4 v[104:107], v2, s[52:53] offset:-512 sc1 nt
	s_mov_b64 exec, s[70:71]
	global_load_dwordx4 v[8:11], v2, s[52:53] sc1 nt
	global_load_dwordx4 v[40:43], v2, s[52:53] offset:512 sc1 nt
	global_load_dwordx4 v[72:75], v2, s[52:53] offset:1024 sc1 nt
	v_mov_b32_e32 v108, 0
	v_mov_b32_e32 v109, 0
	v_mov_b32_e32 v110, 0
	v_mov_b32_e32 v111, 0
	s_mov_b64 s[70:71], exec
	s_mov_b64 exec, s[76:77]
	global_load_dwordx4 v[108:111], v2, s[54:55] offset:-512 sc1 nt
	s_mov_b64 exec, s[70:71]
	global_load_dwordx4 v[12:15], v2, s[54:55] sc1 nt
	global_load_dwordx4 v[44:47], v2, s[54:55] offset:512 sc1 nt
	global_load_dwordx4 v[76:79], v2, s[54:55] offset:1024 sc1 nt
	v_mov_b32_e32 v112, 0
	v_mov_b32_e32 v113, 0
	v_mov_b32_e32 v114, 0
	v_mov_b32_e32 v115, 0
	s_mov_b64 s[70:71], exec
	s_mov_b64 exec, s[76:77]
	global_load_dwordx4 v[112:115], v2, s[56:57] offset:-512 sc1 nt
	s_mov_b64 exec, s[70:71]
	global_load_dwordx4 v[16:19], v2, s[56:57] sc1 nt
	global_load_dwordx4 v[48:51], v2, s[56:57] offset:512 sc1 nt
	global_load_dwordx4 v[80:83], v2, s[56:57] offset:1024 sc1 nt
	v_mov_b32_e32 v116, 0
	v_mov_b32_e32 v117, 0
	v_mov_b32_e32 v118, 0
	v_mov_b32_e32 v119, 0
	s_mov_b64 s[70:71], exec
	s_mov_b64 exec, s[76:77]
	global_load_dwordx4 v[116:119], v2, s[58:59] offset:-512 sc1 nt
	s_mov_b64 exec, s[70:71]
	global_load_dwordx4 v[20:23], v2, s[58:59] sc1 nt
	global_load_dwordx4 v[52:55], v2, s[58:59] offset:512 sc1 nt
	global_load_dwordx4 v[84:87], v2, s[58:59] offset:1024 sc1 nt
	v_mov_b32_e32 v120, 0
	v_mov_b32_e32 v121, 0
	v_mov_b32_e32 v122, 0
	v_mov_b32_e32 v123, 0
	s_mov_b64 s[70:71], exec
	s_mov_b64 exec, s[76:77]
	global_load_dwordx4 v[120:123], v2, s[60:61] offset:-512 sc1 nt
	s_mov_b64 exec, s[70:71]
	global_load_dwordx4 v[24:27], v2, s[60:61] sc1 nt
	global_load_dwordx4 v[56:59], v2, s[60:61] offset:512 sc1 nt
	global_load_dwordx4 v[88:91], v2, s[60:61] offset:1024 sc1 nt
	v_mov_b32_e32 v124, 0
	v_mov_b32_e32 v125, 0
	v_mov_b32_e32 v126, 0
	v_mov_b32_e32 v127, 0
	s_mov_b64 s[70:71], exec
	s_mov_b64 exec, s[76:77]
	global_load_dwordx4 v[124:127], v2, s[62:63] offset:-512 sc1 nt
	s_mov_b64 exec, s[70:71]
	global_load_dwordx4 v[28:31], v2, s[62:63] sc1 nt
	global_load_dwordx4 v[60:63], v2, s[62:63] offset:512 sc1 nt
	global_load_dwordx4 v[92:95], v2, s[62:63] offset:1024 sc1 nt
	v_mov_b32_e32 v128, 0
	v_mov_b32_e32 v129, 0
	v_mov_b32_e32 v130, 0
	v_mov_b32_e32 v131, 0
	s_mov_b64 s[70:71], exec
	s_mov_b64 exec, s[76:77]
	global_load_dwordx4 v[128:131], v2, s[64:65] offset:-512 sc1 nt
	s_mov_b64 exec, s[70:71]
	global_load_dwordx4 v[32:35], v2, s[64:65] sc1 nt
	global_load_dwordx4 v[64:67], v2, s[64:65] offset:512 sc1 nt
	global_load_dwordx4 v[96:99], v2, s[64:65] offset:1024 sc1 nt
	v_mov_b32_e32 v132, 0
	v_mov_b32_e32 v133, 0
	v_mov_b32_e32 v134, 0
	v_mov_b32_e32 v135, 0
	s_mov_b64 s[70:71], exec
	s_mov_b64 exec, s[76:77]
	global_load_dwordx4 v[132:135], v2, s[66:67] offset:-512 sc1 nt
	s_mov_b64 exec, s[70:71]
	global_load_dwordx4 v[36:39], v2, s[66:67] sc1 nt
	global_load_dwordx4 v[68:71], v2, s[66:67] offset:512 sc1 nt
	global_load_dwordx4 v[100:103], v2, s[66:67] offset:1024 sc1 nt
	s_waitcnt vmcnt(31)
	v_cvt_pk_f16_f32 v4, v104, v105
	v_cvt_pk_f16_f32 v5, v106, v107
	s_mov_b64 s[70:71], exec
	s_mov_b64 exec, s[76:77]
	ds_write_b64 v144, v[4:5]
	s_mov_b64 exec, s[70:71]
	global_load_dwordx4 v[104:107], v2, s[52:53] offset:1536 sc1 nt
	s_waitcnt vmcnt(28)
	v_cvt_pk_f16_f32 v4, v108, v109
	v_cvt_pk_f16_f32 v5, v110, v111
	s_mov_b64 s[70:71], exec
	s_mov_b64 exec, s[76:77]
	ds_write_b64 v144, v[4:5] offset:2176
	s_mov_b64 exec, s[70:71]
	global_load_dwordx4 v[108:111], v2, s[54:55] offset:1536 sc1 nt
	s_waitcnt vmcnt(25)
	v_cvt_pk_f16_f32 v4, v112, v113
	v_cvt_pk_f16_f32 v5, v114, v115
	s_mov_b64 s[70:71], exec
	s_mov_b64 exec, s[76:77]
	ds_write_b64 v144, v[4:5] offset:4352
	s_mov_b64 exec, s[70:71]
	global_load_dwordx4 v[112:115], v2, s[56:57] offset:1536 sc1 nt
	s_waitcnt vmcnt(22)
	v_cvt_pk_f16_f32 v4, v116, v117
	v_cvt_pk_f16_f32 v5, v118, v119
	s_mov_b64 s[70:71], exec
	s_mov_b64 exec, s[76:77]
	ds_write_b64 v144, v[4:5] offset:6528
	s_mov_b64 exec, s[70:71]
	global_load_dwordx4 v[116:119], v2, s[58:59] offset:1536 sc1 nt
	s_waitcnt vmcnt(19)
	v_cvt_pk_f16_f32 v4, v120, v121
	v_cvt_pk_f16_f32 v5, v122, v123
	s_mov_b64 s[70:71], exec
	s_mov_b64 exec, s[76:77]
	ds_write_b64 v144, v[4:5] offset:8704
	s_mov_b64 exec, s[70:71]
	global_load_dwordx4 v[120:123], v2, s[60:61] offset:1536 sc1 nt
	s_waitcnt vmcnt(16)
	v_cvt_pk_f16_f32 v4, v124, v125
	v_cvt_pk_f16_f32 v5, v126, v127
	s_mov_b64 s[70:71], exec
	s_mov_b64 exec, s[76:77]
	ds_write_b64 v144, v[4:5] offset:10880
	s_mov_b64 exec, s[70:71]
	global_load_dwordx4 v[124:127], v2, s[62:63] offset:1536 sc1 nt
	s_waitcnt vmcnt(13)
	v_cvt_pk_f16_f32 v4, v128, v129
	v_cvt_pk_f16_f32 v5, v130, v131
	s_mov_b64 s[70:71], exec
	s_mov_b64 exec, s[76:77]
	ds_write_b64 v144, v[4:5] offset:13056
	s_mov_b64 exec, s[70:71]
	global_load_dwordx4 v[128:131], v2, s[64:65] offset:1536 sc1 nt
	s_waitcnt vmcnt(10)
	v_cvt_pk_f16_f32 v4, v132, v133
	v_cvt_pk_f16_f32 v5, v134, v135
	s_mov_b64 s[70:71], exec
	s_mov_b64 exec, s[76:77]
	ds_write_b64 v144, v[4:5] offset:15232
	s_mov_b64 exec, s[70:71]
	global_load_dwordx4 v[132:135], v2, s[66:67] offset:1536 sc1 nt
	s_waitcnt vmcnt(40)
	v_mov_b32_e32 v151, 1
	v_lshlrev_b32_e32 v160, 2, v152
	v_lshlrev_b32_e32 v161, 2, v153
	v_lshlrev_b32_e32 v162, 2, v154
	v_lshlrev_b32_e32 v163, 2, v155
	global_atomic_add v164, v160, v151, s[20:21] sc0
	global_atomic_add v165, v161, v151, s[20:21] sc0
	global_atomic_add v166, v162, v151, s[20:21] sc0
	global_atomic_add v167, v163, v151, s[20:21] sc0
	s_waitcnt vmcnt(42)
	v_cvt_pk_f16_f32 v4, v8, v9
	v_cvt_pk_f16_f32 v5, v10, v11
	ds_write_b64 v141, v[4:5]
	s_waitcnt vmcnt(41)
	v_cvt_pk_f16_f32 v4, v40, v41
	v_cvt_pk_f16_f32 v5, v42, v43
	ds_write_b64 v142, v[4:5]
	global_load_dwordx4 v[8:11], v2, s[52:53] offset:2048 sc1 nt
	global_load_dwordx4 v[40:43], v2, s[52:53] offset:2560 sc1 nt
	s_waitcnt vmcnt(40)
	v_cvt_pk_f16_f32 v4, v12, v13
	v_cvt_pk_f16_f32 v5, v14, v15
	ds_write_b64 v141, v[4:5] offset:2176
	s_waitcnt vmcnt(39)
	v_cvt_pk_f16_f32 v4, v44, v45
	v_cvt_pk_f16_f32 v5, v46, v47
	ds_write_b64 v142, v[4:5] offset:2176
	global_load_dwordx4 v[12:15], v2, s[54:55] offset:2048 sc1 nt
	global_load_dwordx4 v[44:47], v2, s[54:55] offset:2560 sc1 nt
	s_waitcnt vmcnt(38)
	v_cvt_pk_f16_f32 v4, v16, v17
	v_cvt_pk_f16_f32 v5, v18, v19
	ds_write_b64 v141, v[4:5] offset:4352
	s_waitcnt vmcnt(37)
	v_cvt_pk_f16_f32 v4, v48, v49
	v_cvt_pk_f16_f32 v5, v50, v51
	ds_write_b64 v142, v[4:5] offset:4352
	global_load_dwordx4 v[16:19], v2, s[56:57] offset:2048 sc1 nt
	global_load_dwordx4 v[48:51], v2, s[56:57] offset:2560 sc1 nt
	s_waitcnt vmcnt(36)
	v_cvt_pk_f16_f32 v4, v20, v21
	v_cvt_pk_f16_f32 v5, v22, v23
	ds_write_b64 v141, v[4:5] offset:6528
	s_waitcnt vmcnt(35)
	v_cvt_pk_f16_f32 v4, v52, v53
	v_cvt_pk_f16_f32 v5, v54, v55
	ds_write_b64 v142, v[4:5] offset:6528
	global_load_dwordx4 v[20:23], v2, s[58:59] offset:2048 sc1 nt
	global_load_dwordx4 v[52:55], v2, s[58:59] offset:2560 sc1 nt
	s_waitcnt vmcnt(34)
	v_cvt_pk_f16_f32 v4, v24, v25
	v_cvt_pk_f16_f32 v5, v26, v27
	ds_write_b64 v141, v[4:5] offset:8704
	s_waitcnt vmcnt(33)
	v_cvt_pk_f16_f32 v4, v56, v57
	v_cvt_pk_f16_f32 v5, v58, v59
	ds_write_b64 v142, v[4:5] offset:8704
	global_load_dwordx4 v[24:27], v2, s[60:61] offset:2048 sc1 nt
	global_load_dwordx4 v[56:59], v2, s[60:61] offset:2560 sc1 nt
	s_waitcnt vmcnt(32)
	v_cvt_pk_f16_f32 v4, v28, v29
	v_cvt_pk_f16_f32 v5, v30, v31
	ds_write_b64 v141, v[4:5] offset:10880
	s_waitcnt vmcnt(31)
	v_cvt_pk_f16_f32 v4, v60, v61
	v_cvt_pk_f16_f32 v5, v62, v63
	ds_write_b64 v142, v[4:5] offset:10880
	global_load_dwordx4 v[28:31], v2, s[62:63] offset:2048 sc1 nt
	global_load_dwordx4 v[60:63], v2, s[62:63] offset:2560 sc1 nt
	s_waitcnt vmcnt(30)
	v_cvt_pk_f16_f32 v4, v32, v33
	v_cvt_pk_f16_f32 v5, v34, v35
	ds_write_b64 v141, v[4:5] offset:13056
	s_waitcnt vmcnt(29)
	v_cvt_pk_f16_f32 v4, v64, v65
	v_cvt_pk_f16_f32 v5, v66, v67
	ds_write_b64 v142, v[4:5] offset:13056
	global_load_dwordx4 v[32:35], v2, s[64:65] offset:2048 sc1 nt
	global_load_dwordx4 v[64:67], v2, s[64:65] offset:2560 sc1 nt
	s_waitcnt vmcnt(28)
	v_cvt_pk_f16_f32 v4, v36, v37
	v_cvt_pk_f16_f32 v5, v38, v39
	ds_write_b64 v141, v[4:5] offset:15232
	s_waitcnt vmcnt(27)
	v_cvt_pk_f16_f32 v4, v68, v69
	v_cvt_pk_f16_f32 v5, v70, v71
	ds_write_b64 v142, v[4:5] offset:15232
	global_load_dwordx4 v[36:39], v2, s[66:67] offset:2048 sc1 nt
	global_load_dwordx4 v[68:71], v2, s[66:67] offset:2560 sc1 nt
	s_waitcnt vmcnt(0)
	v_cmp_gt_i32_e32 vcc, 64, v164
	v_lshl_add_u32 v148, v152, 6, v164
	v_lshlrev_b32_e32 v148, 2, v148
	s_and_saveexec_b64 s[2:3], vcc
	global_store_dword v148, v156, s[22:23]
	s_xor_b64 exec, exec, s[2:3]
	s_cbranch_execz .Lg1_ld_ok_0
	v_mov_b32_e32 v149, 0x8000
	global_atomic_add v149, v149, v151, s[20:21] sc0
	s_waitcnt vmcnt(0)
	v_lshlrev_b32_e32 v149, 3, v149
	v_mov_b32_e32 v160, v152
	v_mov_b32_e32 v161, v156
	global_store_dwordx2 v149, v[160:161], s[28:29]

.Lg1_ld_ok_3:
	s_mov_b64 exec, -1
	s_waitcnt lgkmcnt(0)
	s_barrier
	s_waitcnt lgkmcnt(0)
	s_barrier
	s_waitcnt vmcnt(56)
	v_cvt_pk_f16_f32 v4, v72, v73
	v_cvt_pk_f16_f32 v5, v74, v75
	ds_write_b64 v143, v[4:5]
	s_waitcnt vmcnt(27)
	v_cvt_pk_f16_f32 v4, v104, v105
	v_cvt_pk_f16_f32 v5, v106, v107
	ds_write_b64 v144, v[4:5]
	global_load_dwordx4 v[72:75], v2, s[52:53] offset:3072 sc1 nt
	global_load_dwordx4 v[104:107], v2, s[52:53] offset:3584 sc1 nt
	s_waitcnt vmcnt(54)
	v_cvt_pk_f16_f32 v4, v76, v77
	v_cvt_pk_f16_f32 v5, v78, v79
	ds_write_b64 v143, v[4:5] offset:2176
	s_waitcnt vmcnt(28)
	v_cvt_pk_f16_f32 v4, v108, v109
	v_cvt_pk_f16_f32 v5, v110, v111
	ds_write_b64 v144, v[4:5] offset:2176
	global_load_dwordx4 v[76:79], v2, s[54:55] offset:3072 sc1 nt
	global_load_dwordx4 v[108:111], v2, s[54:55] offset:3584 sc1 nt
	s_waitcnt vmcnt(52)
	v_cvt_pk_f16_f32 v4, v80, v81
	v_cvt_pk_f16_f32 v5, v82, v83
	ds_write_b64 v143, v[4:5] offset:4352
	s_waitcnt vmcnt(29)
	v_cvt_pk_f16_f32 v4, v112, v113
	v_cvt_pk_f16_f32 v5, v114, v115
	ds_write_b64 v144, v[4:5] offset:4352
	global_load_dwordx4 v[80:83], v2, s[56:57] offset:3072 sc1 nt
	global_load_dwordx4 v[112:115], v2, s[56:57] offset:3584 sc1 nt
	s_waitcnt vmcnt(50)
	v_cvt_pk_f16_f32 v4, v84, v85
	v_cvt_pk_f16_f32 v5, v86, v87
	ds_write_b64 v143, v[4:5] offset:6528
	s_waitcnt vmcnt(30)
	v_cvt_pk_f16_f32 v4, v116, v117
	v_cvt_pk_f16_f32 v5, v118, v119
	ds_write_b64 v144, v[4:5] offset:6528
	global_load_dwordx4 v[84:87], v2, s[58:59] offset:3072 sc1 nt
	global_load_dwordx4 v[116:119], v2, s[58:59] offset:3584 sc1 nt
	s_waitcnt vmcnt(48)
	v_cvt_pk_f16_f32 v4, v88, v89
	v_cvt_pk_f16_f32 v5, v90, v91
	ds_write_b64 v143, v[4:5] offset:8704
	s_waitcnt vmcnt(31)
	v_cvt_pk_f16_f32 v4, v120, v121
	v_cvt_pk_f16_f32 v5, v122, v123
	ds_write_b64 v144, v[4:5] offset:8704
	global_load_dwordx4 v[88:91], v2, s[60:61] offset:3072 sc1 nt
	global_load_dwordx4 v[120:123], v2, s[60:61] offset:3584 sc1 nt
	s_waitcnt vmcnt(46)
	v_cvt_pk_f16_f32 v4, v92, v93
	v_cvt_pk_f16_f32 v5, v94, v95
	ds_write_b64 v143, v[4:5] offset:10880
	s_waitcnt vmcnt(32)
	v_cvt_pk_f16_f32 v4, v124, v125
	v_cvt_pk_f16_f32 v5, v126, v127
	ds_write_b64 v144, v[4:5] offset:10880
	global_load_dwordx4 v[92:95], v2, s[62:63] offset:3072 sc1 nt
	global_load_dwordx4 v[124:127], v2, s[62:63] offset:3584 sc1 nt
	s_waitcnt vmcnt(44)
	v_cvt_pk_f16_f32 v4, v96, v97
	v_cvt_pk_f16_f32 v5, v98, v99
	ds_write_b64 v143, v[4:5] offset:13056
	s_waitcnt vmcnt(33)
	v_cvt_pk_f16_f32 v4, v128, v129
	v_cvt_pk_f16_f32 v5, v130, v131
	ds_write_b64 v144, v[4:5] offset:13056
	global_load_dwordx4 v[96:99], v2, s[64:65] offset:3072 sc1 nt
	global_load_dwordx4 v[128:131], v2, s[64:65] offset:3584 sc1 nt
	s_waitcnt vmcnt(42)
	v_cvt_pk_f16_f32 v4, v100, v101
	v_cvt_pk_f16_f32 v5, v102, v103
	ds_write_b64 v143, v[4:5] offset:15232
	s_waitcnt vmcnt(34)
	v_cvt_pk_f16_f32 v4, v132, v133
	v_cvt_pk_f16_f32 v5, v134, v135
	ds_write_b64 v144, v[4:5] offset:15232
	global_load_dwordx4 v[100:103], v2, s[66:67] offset:3072 sc1 nt
	global_load_dwordx4 v[132:135], v2, s[66:67] offset:3584 sc1 nt
	s_waitcnt lgkmcnt(0)
	s_barrier
	s_waitcnt lgkmcnt(0)
	s_barrier
	s_waitcnt vmcnt(31)
	v_cvt_pk_f16_f32 v4, v8, v9
	v_cvt_pk_f16_f32 v5, v10, v11
	ds_write_b64 v141, v[4:5]
	s_waitcnt vmcnt(30)
	v_cvt_pk_f16_f32 v4, v40, v41
	v_cvt_pk_f16_f32 v5, v42, v43
	ds_write_b64 v142, v[4:5]
	v_add_u32_e32 v2, 0x1000, v2
	global_load_dwordx4 v[8:11], v2, s[52:53] sc1 nt
	global_load_dwordx4 v[40:43], v2, s[52:53] offset:512 sc1 nt
	s_waitcnt vmcnt(31)
	v_cvt_pk_f16_f32 v4, v12, v13
	v_cvt_pk_f16_f32 v5, v14, v15
	ds_write_b64 v141, v[4:5] offset:2176
	s_waitcnt vmcnt(30)
	v_cvt_pk_f16_f32 v4, v44, v45
	v_cvt_pk_f16_f32 v5, v46, v47
	ds_write_b64 v142, v[4:5] offset:2176
	global_load_dwordx4 v[12:15], v2, s[54:55] sc1 nt
	global_load_dwordx4 v[44:47], v2, s[54:55] offset:512 sc1 nt
	s_waitcnt vmcnt(31)
	v_cvt_pk_f16_f32 v4, v16, v17
	v_cvt_pk_f16_f32 v5, v18, v19
	ds_write_b64 v141, v[4:5] offset:4352
	s_waitcnt vmcnt(30)
	v_cvt_pk_f16_f32 v4, v48, v49
	v_cvt_pk_f16_f32 v5, v50, v51
	ds_write_b64 v142, v[4:5] offset:4352
	global_load_dwordx4 v[16:19], v2, s[56:57] sc1 nt
	global_load_dwordx4 v[48:51], v2, s[56:57] offset:512 sc1 nt
	s_waitcnt vmcnt(31)
	v_cvt_pk_f16_f32 v4, v20, v21
	v_cvt_pk_f16_f32 v5, v22, v23
	ds_write_b64 v141, v[4:5] offset:6528
	s_waitcnt vmcnt(30)
	v_cvt_pk_f16_f32 v4, v52, v53
	v_cvt_pk_f16_f32 v5, v54, v55
	ds_write_b64 v142, v[4:5] offset:6528
	global_load_dwordx4 v[20:23], v2, s[58:59] sc1 nt
	global_load_dwordx4 v[52:55], v2, s[58:59] offset:512 sc1 nt
	s_waitcnt vmcnt(31)
	v_cvt_pk_f16_f32 v4, v24, v25
	v_cvt_pk_f16_f32 v5, v26, v27
	ds_write_b64 v141, v[4:5] offset:8704
	s_waitcnt vmcnt(30)
	v_cvt_pk_f16_f32 v4, v56, v57
	v_cvt_pk_f16_f32 v5, v58, v59
	ds_write_b64 v142, v[4:5] offset:8704
	global_load_dwordx4 v[24:27], v2, s[60:61] sc1 nt
	global_load_dwordx4 v[56:59], v2, s[60:61] offset:512 sc1 nt
	s_waitcnt vmcnt(31)
	v_cvt_pk_f16_f32 v4, v28, v29
	v_cvt_pk_f16_f32 v5, v30, v31
	ds_write_b64 v141, v[4:5] offset:10880
	s_waitcnt vmcnt(30)
	v_cvt_pk_f16_f32 v4, v60, v61
	v_cvt_pk_f16_f32 v5, v62, v63
	ds_write_b64 v142, v[4:5] offset:10880
	global_load_dwordx4 v[28:31], v2, s[62:63] sc1 nt
	global_load_dwordx4 v[60:63], v2, s[62:63] offset:512 sc1 nt
	s_waitcnt vmcnt(31)
	v_cvt_pk_f16_f32 v4, v32, v33
	v_cvt_pk_f16_f32 v5, v34, v35
	ds_write_b64 v141, v[4:5] offset:13056
	s_waitcnt vmcnt(30)
	v_cvt_pk_f16_f32 v4, v64, v65
	v_cvt_pk_f16_f32 v5, v66, v67
	ds_write_b64 v142, v[4:5] offset:13056
	global_load_dwordx4 v[32:35], v2, s[64:65] sc1 nt
	global_load_dwordx4 v[64:67], v2, s[64:65] offset:512 sc1 nt
	s_waitcnt vmcnt(31)
	v_cvt_pk_f16_f32 v4, v36, v37
	v_cvt_pk_f16_f32 v5, v38, v39
	ds_write_b64 v141, v[4:5] offset:15232
	s_waitcnt vmcnt(30)
	v_cvt_pk_f16_f32 v4, v68, v69
	v_cvt_pk_f16_f32 v5, v70, v71
	ds_write_b64 v142, v[4:5] offset:15232
	global_load_dwordx4 v[36:39], v2, s[66:67] sc1 nt
	global_load_dwordx4 v[68:71], v2, s[66:67] offset:512 sc1 nt
	s_waitcnt lgkmcnt(0)
	s_barrier
	s_waitcnt lgkmcnt(0)
	s_barrier
	s_waitcnt vmcnt(31)
	v_cvt_pk_f16_f32 v4, v72, v73
	v_cvt_pk_f16_f32 v5, v74, v75
	ds_write_b64 v143, v[4:5]
	s_waitcnt vmcnt(30)
	v_cvt_pk_f16_f32 v4, v104, v105
	v_cvt_pk_f16_f32 v5, v106, v107
	ds_write_b64 v144, v[4:5]
	global_load_dwordx4 v[72:75], v2, s[52:53] offset:1024 sc1 nt
	global_load_dwordx4 v[104:107], v2, s[52:53] offset:1536 sc1 nt
	s_waitcnt vmcnt(31)
	v_cvt_pk_f16_f32 v4, v76, v77
	v_cvt_pk_f16_f32 v5, v78, v79
	ds_write_b64 v143, v[4:5] offset:2176
	s_waitcnt vmcnt(30)
	v_cvt_pk_f16_f32 v4, v108, v109
	v_cvt_pk_f16_f32 v5, v110, v111
	ds_write_b64 v144, v[4:5] offset:2176
	global_load_dwordx4 v[76:79], v2, s[54:55] offset:1024 sc1 nt
	global_load_dwordx4 v[108:111], v2, s[54:55] offset:1536 sc1 nt
	s_waitcnt vmcnt(31)
	v_cvt_pk_f16_f32 v4, v80, v81
	v_cvt_pk_f16_f32 v5, v82, v83
	ds_write_b64 v143, v[4:5] offset:4352
	s_waitcnt vmcnt(30)
	v_cvt_pk_f16_f32 v4, v112, v113
	v_cvt_pk_f16_f32 v5, v114, v115
	ds_write_b64 v144, v[4:5] offset:4352
	global_load_dwordx4 v[80:83], v2, s[56:57] offset:1024 sc1 nt
	global_load_dwordx4 v[112:115], v2, s[56:57] offset:1536 sc1 nt
	s_waitcnt vmcnt(31)
	v_cvt_pk_f16_f32 v4, v84, v85
	v_cvt_pk_f16_f32 v5, v86, v87
	ds_write_b64 v143, v[4:5] offset:6528
	s_waitcnt vmcnt(30)
	v_cvt_pk_f16_f32 v4, v116, v117
	v_cvt_pk_f16_f32 v5, v118, v119
	ds_write_b64 v144, v[4:5] offset:6528
	global_load_dwordx4 v[84:87], v2, s[58:59] offset:1024 sc1 nt
	global_load_dwordx4 v[116:119], v2, s[58:59] offset:1536 sc1 nt
	s_waitcnt vmcnt(31)
	v_cvt_pk_f16_f32 v4, v88, v89
	v_cvt_pk_f16_f32 v5, v90, v91
	ds_write_b64 v143, v[4:5] offset:8704
	s_waitcnt vmcnt(30)
	v_cvt_pk_f16_f32 v4, v120, v121
	v_cvt_pk_f16_f32 v5, v122, v123
	ds_write_b64 v144, v[4:5] offset:8704
	global_load_dwordx4 v[88:91], v2, s[60:61] offset:1024 sc1 nt
	global_load_dwordx4 v[120:123], v2, s[60:61] offset:1536 sc1 nt
	s_waitcnt vmcnt(31)
	v_cvt_pk_f16_f32 v4, v92, v93
	v_cvt_pk_f16_f32 v5, v94, v95
	ds_write_b64 v143, v[4:5] offset:10880
	s_waitcnt vmcnt(30)
	v_cvt_pk_f16_f32 v4, v124, v125
	v_cvt_pk_f16_f32 v5, v126, v127
	ds_write_b64 v144, v[4:5] offset:10880
	global_load_dwordx4 v[92:95], v2, s[62:63] offset:1024 sc1 nt
	global_load_dwordx4 v[124:127], v2, s[62:63] offset:1536 sc1 nt
	s_waitcnt vmcnt(31)
	v_cvt_pk_f16_f32 v4, v96, v97
	v_cvt_pk_f16_f32 v5, v98, v99
	ds_write_b64 v143, v[4:5] offset:13056
	s_waitcnt vmcnt(30)
	v_cvt_pk_f16_f32 v4, v128, v129
	v_cvt_pk_f16_f32 v5, v130, v131
	ds_write_b64 v144, v[4:5] offset:13056
	global_load_dwordx4 v[96:99], v2, s[64:65] offset:1024 sc1 nt
	global_load_dwordx4 v[128:131], v2, s[64:65] offset:1536 sc1 nt
	s_waitcnt vmcnt(31)
	v_cvt_pk_f16_f32 v4, v100, v101
	v_cvt_pk_f16_f32 v5, v102, v103
	ds_write_b64 v143, v[4:5] offset:15232
	s_waitcnt vmcnt(30)
	v_cvt_pk_f16_f32 v4, v132, v133
	v_cvt_pk_f16_f32 v5, v134, v135
	ds_write_b64 v144, v[4:5] offset:15232
	global_load_dwordx4 v[100:103], v2, s[66:67] offset:1024 sc1 nt
	global_load_dwordx4 v[132:135], v2, s[66:67] offset:1536 sc1 nt
	s_waitcnt lgkmcnt(0)
	s_barrier
	s_waitcnt lgkmcnt(0)
	s_barrier
	s_waitcnt vmcnt(31)
	v_cvt_pk_f16_f32 v4, v8, v9
	v_cvt_pk_f16_f32 v5, v10, v11
	ds_write_b64 v141, v[4:5]
	s_waitcnt vmcnt(30)
	v_cvt_pk_f16_f32 v4, v40, v41
	v_cvt_pk_f16_f32 v5, v42, v43
	ds_write_b64 v142, v[4:5]
	global_load_dwordx4 v[8:11], v2, s[52:53] offset:2048 sc1 nt
	global_load_dwordx4 v[40:43], v2, s[52:53] offset:2560 sc1 nt
	s_waitcnt vmcnt(31)
	v_cvt_pk_f16_f32 v4, v12, v13
	v_cvt_pk_f16_f32 v5, v14, v15
	ds_write_b64 v141, v[4:5] offset:2176
	s_waitcnt vmcnt(30)
	v_cvt_pk_f16_f32 v4, v44, v45
	v_cvt_pk_f16_f32 v5, v46, v47
	ds_write_b64 v142, v[4:5] offset:2176
	global_load_dwordx4 v[12:15], v2, s[54:55] offset:2048 sc1 nt
	global_load_dwordx4 v[44:47], v2, s[54:55] offset:2560 sc1 nt
	s_waitcnt vmcnt(31)
	v_cvt_pk_f16_f32 v4, v16, v17
	v_cvt_pk_f16_f32 v5, v18, v19
	ds_write_b64 v141, v[4:5] offset:4352
	s_waitcnt vmcnt(30)
	v_cvt_pk_f16_f32 v4, v48, v49
	v_cvt_pk_f16_f32 v5, v50, v51
	ds_write_b64 v142, v[4:5] offset:4352
	global_load_dwordx4 v[16:19], v2, s[56:57] offset:2048 sc1 nt
	global_load_dwordx4 v[48:51], v2, s[56:57] offset:2560 sc1 nt
	s_waitcnt vmcnt(31)
	v_cvt_pk_f16_f32 v4, v20, v21
	v_cvt_pk_f16_f32 v5, v22, v23
	ds_write_b64 v141, v[4:5] offset:6528
	s_waitcnt vmcnt(30)
	v_cvt_pk_f16_f32 v4, v52, v53
	v_cvt_pk_f16_f32 v5, v54, v55
	ds_write_b64 v142, v[4:5] offset:6528
	global_load_dwordx4 v[20:23], v2, s[58:59] offset:2048 sc1 nt
	global_load_dwordx4 v[52:55], v2, s[58:59] offset:2560 sc1 nt
	s_waitcnt vmcnt(31)
	v_cvt_pk_f16_f32 v4, v24, v25
	v_cvt_pk_f16_f32 v5, v26, v27
	ds_write_b64 v141, v[4:5] offset:8704
	s_waitcnt vmcnt(30)
	v_cvt_pk_f16_f32 v4, v56, v57
	v_cvt_pk_f16_f32 v5, v58, v59
	ds_write_b64 v142, v[4:5] offset:8704
	global_load_dwordx4 v[24:27], v2, s[60:61] offset:2048 sc1 nt
	global_load_dwordx4 v[56:59], v2, s[60:61] offset:2560 sc1 nt
	s_waitcnt vmcnt(31)
	v_cvt_pk_f16_f32 v4, v28, v29
	v_cvt_pk_f16_f32 v5, v30, v31
	ds_write_b64 v141, v[4:5] offset:10880
	s_waitcnt vmcnt(30)
	v_cvt_pk_f16_f32 v4, v60, v61
	v_cvt_pk_f16_f32 v5, v62, v63
	ds_write_b64 v142, v[4:5] offset:10880
	global_load_dwordx4 v[28:31], v2, s[62:63] offset:2048 sc1 nt
	global_load_dwordx4 v[60:63], v2, s[62:63] offset:2560 sc1 nt
	s_waitcnt vmcnt(31)
	v_cvt_pk_f16_f32 v4, v32, v33
	v_cvt_pk_f16_f32 v5, v34, v35
	ds_write_b64 v141, v[4:5] offset:13056
	s_waitcnt vmcnt(30)
	v_cvt_pk_f16_f32 v4, v64, v65
	v_cvt_pk_f16_f32 v5, v66, v67
	ds_write_b64 v142, v[4:5] offset:13056
	global_load_dwordx4 v[32:35], v2, s[64:65] offset:2048 sc1 nt
	global_load_dwordx4 v[64:67], v2, s[64:65] offset:2560 sc1 nt
	s_waitcnt vmcnt(31)
	v_cvt_pk_f16_f32 v4, v36, v37
	v_cvt_pk_f16_f32 v5, v38, v39
	ds_write_b64 v141, v[4:5] offset:15232
	s_waitcnt vmcnt(30)
	v_cvt_pk_f16_f32 v4, v68, v69
	v_cvt_pk_f16_f32 v5, v70, v71
	ds_write_b64 v142, v[4:5] offset:15232
	global_load_dwordx4 v[36:39], v2, s[66:67] offset:2048 sc1 nt
	global_load_dwordx4 v[68:71], v2, s[66:67] offset:2560 sc1 nt
	s_waitcnt lgkmcnt(0)
	s_barrier
	s_waitcnt lgkmcnt(0)
	s_barrier
	s_waitcnt vmcnt(31)
	v_cvt_pk_f16_f32 v4, v72, v73
	v_cvt_pk_f16_f32 v5, v74, v75
	ds_write_b64 v143, v[4:5]
	s_waitcnt vmcnt(30)
	v_cvt_pk_f16_f32 v4, v104, v105
	v_cvt_pk_f16_f32 v5, v106, v107
	ds_write_b64 v144, v[4:5]
	global_load_dwordx4 v[72:75], v2, s[52:53] offset:3072 sc1 nt
	global_load_dwordx4 v[104:107], v2, s[52:53] offset:3584 sc1 nt
	s_waitcnt vmcnt(31)
	v_cvt_pk_f16_f32 v4, v76, v77
	v_cvt_pk_f16_f32 v5, v78, v79
	ds_write_b64 v143, v[4:5] offset:2176
	s_waitcnt vmcnt(30)
	v_cvt_pk_f16_f32 v4, v108, v109
	v_cvt_pk_f16_f32 v5, v110, v111
	ds_write_b64 v144, v[4:5] offset:2176
	global_load_dwordx4 v[76:79], v2, s[54:55] offset:3072 sc1 nt
	global_load_dwordx4 v[108:111], v2, s[54:55] offset:3584 sc1 nt
	s_waitcnt vmcnt(31)
	v_cvt_pk_f16_f32 v4, v80, v81
	v_cvt_pk_f16_f32 v5, v82, v83
	ds_write_b64 v143, v[4:5] offset:4352
	s_waitcnt vmcnt(30)
	v_cvt_pk_f16_f32 v4, v112, v113
	v_cvt_pk_f16_f32 v5, v114, v115
	ds_write_b64 v144, v[4:5] offset:4352
	global_load_dwordx4 v[80:83], v2, s[56:57] offset:3072 sc1 nt
	global_load_dwordx4 v[112:115], v2, s[56:57] offset:3584 sc1 nt
	s_waitcnt vmcnt(31)
	v_cvt_pk_f16_f32 v4, v84, v85
	v_cvt_pk_f16_f32 v5, v86, v87
	ds_write_b64 v143, v[4:5] offset:6528
	s_waitcnt vmcnt(30)
	v_cvt_pk_f16_f32 v4, v116, v117
	v_cvt_pk_f16_f32 v5, v118, v119
	ds_write_b64 v144, v[4:5] offset:6528
	global_load_dwordx4 v[84:87], v2, s[58:59] offset:3072 sc1 nt
	global_load_dwordx4 v[116:119], v2, s[58:59] offset:3584 sc1 nt
	s_waitcnt vmcnt(31)
	v_cvt_pk_f16_f32 v4, v88, v89
	v_cvt_pk_f16_f32 v5, v90, v91
	ds_write_b64 v143, v[4:5] offset:8704
	s_waitcnt vmcnt(30)
	v_cvt_pk_f16_f32 v4, v120, v121
	v_cvt_pk_f16_f32 v5, v122, v123
	ds_write_b64 v144, v[4:5] offset:8704
	global_load_dwordx4 v[88:91], v2, s[60:61] offset:3072 sc1 nt
	global_load_dwordx4 v[120:123], v2, s[60:61] offset:3584 sc1 nt
	s_waitcnt vmcnt(31)
	v_cvt_pk_f16_f32 v4, v92, v93
	v_cvt_pk_f16_f32 v5, v94, v95
	ds_write_b64 v143, v[4:5] offset:10880
	s_waitcnt vmcnt(30)
	v_cvt_pk_f16_f32 v4, v124, v125
	v_cvt_pk_f16_f32 v5, v126, v127
	ds_write_b64 v144, v[4:5] offset:10880
	global_load_dwordx4 v[92:95], v2, s[62:63] offset:3072 sc1 nt
	global_load_dwordx4 v[124:127], v2, s[62:63] offset:3584 sc1 nt
	s_waitcnt vmcnt(31)
	v_cvt_pk_f16_f32 v4, v96, v97
	v_cvt_pk_f16_f32 v5, v98, v99
	ds_write_b64 v143, v[4:5] offset:13056
	s_waitcnt vmcnt(30)
	v_cvt_pk_f16_f32 v4, v128, v129
	v_cvt_pk_f16_f32 v5, v130, v131
	ds_write_b64 v144, v[4:5] offset:13056
	global_load_dwordx4 v[96:99], v2, s[64:65] offset:3072 sc1 nt
	global_load_dwordx4 v[128:131], v2, s[64:65] offset:3584 sc1 nt
	s_waitcnt vmcnt(31)
	v_cvt_pk_f16_f32 v4, v100, v101
	v_cvt_pk_f16_f32 v5, v102, v103
	ds_write_b64 v143, v[4:5] offset:15232
	s_waitcnt vmcnt(30)
	v_cvt_pk_f16_f32 v4, v132, v133
	v_cvt_pk_f16_f32 v5, v134, v135
	ds_write_b64 v144, v[4:5] offset:15232
	global_load_dwordx4 v[100:103], v2, s[66:67] offset:3072 sc1 nt
	global_load_dwordx4 v[132:135], v2, s[66:67] offset:3584 sc1 nt
	s_waitcnt lgkmcnt(0)
	s_barrier
	s_waitcnt lgkmcnt(0)
	s_barrier
	s_waitcnt vmcnt(31)
	v_cvt_pk_f16_f32 v4, v8, v9
	v_cvt_pk_f16_f32 v5, v10, v11
	ds_write_b64 v141, v[4:5]
	s_waitcnt vmcnt(30)
	v_cvt_pk_f16_f32 v4, v40, v41
	v_cvt_pk_f16_f32 v5, v42, v43
	ds_write_b64 v142, v[4:5]
	v_add_u32_e32 v2, 0x1000, v2
	global_load_dwordx4 v[8:11], v2, s[52:53] sc1 nt
	global_load_dwordx4 v[40:43], v2, s[52:53] offset:512 sc1 nt
	s_waitcnt vmcnt(31)
	v_cvt_pk_f16_f32 v4, v12, v13
	v_cvt_pk_f16_f32 v5, v14, v15
	ds_write_b64 v141, v[4:5] offset:2176
	s_waitcnt vmcnt(30)
	v_cvt_pk_f16_f32 v4, v44, v45
	v_cvt_pk_f16_f32 v5, v46, v47
	ds_write_b64 v142, v[4:5] offset:2176
	global_load_dwordx4 v[12:15], v2, s[54:55] sc1 nt
	global_load_dwordx4 v[44:47], v2, s[54:55] offset:512 sc1 nt
	s_waitcnt vmcnt(31)
	v_cvt_pk_f16_f32 v4, v16, v17
	v_cvt_pk_f16_f32 v5, v18, v19
	ds_write_b64 v141, v[4:5] offset:4352
	s_waitcnt vmcnt(30)
	v_cvt_pk_f16_f32 v4, v48, v49
	v_cvt_pk_f16_f32 v5, v50, v51
	ds_write_b64 v142, v[4:5] offset:4352
	global_load_dwordx4 v[16:19], v2, s[56:57] sc1 nt
	global_load_dwordx4 v[48:51], v2, s[56:57] offset:512 sc1 nt
	s_waitcnt vmcnt(31)
	v_cvt_pk_f16_f32 v4, v20, v21
	v_cvt_pk_f16_f32 v5, v22, v23
	ds_write_b64 v141, v[4:5] offset:6528
	s_waitcnt vmcnt(30)
	v_cvt_pk_f16_f32 v4, v52, v53
	v_cvt_pk_f16_f32 v5, v54, v55
	ds_write_b64 v142, v[4:5] offset:6528
	global_load_dwordx4 v[20:23], v2, s[58:59] sc1 nt
	global_load_dwordx4 v[52:55], v2, s[58:59] offset:512 sc1 nt
	s_waitcnt vmcnt(31)
	v_cvt_pk_f16_f32 v4, v24, v25
	v_cvt_pk_f16_f32 v5, v26, v27
	ds_write_b64 v141, v[4:5] offset:8704
	s_waitcnt vmcnt(30)
	v_cvt_pk_f16_f32 v4, v56, v57
	v_cvt_pk_f16_f32 v5, v58, v59
	ds_write_b64 v142, v[4:5] offset:8704
	global_load_dwordx4 v[24:27], v2, s[60:61] sc1 nt
	global_load_dwordx4 v[56:59], v2, s[60:61] offset:512 sc1 nt
	s_waitcnt vmcnt(31)
	v_cvt_pk_f16_f32 v4, v28, v29
	v_cvt_pk_f16_f32 v5, v30, v31
	ds_write_b64 v141, v[4:5] offset:10880
	s_waitcnt vmcnt(30)
	v_cvt_pk_f16_f32 v4, v60, v61
	v_cvt_pk_f16_f32 v5, v62, v63
	ds_write_b64 v142, v[4:5] offset:10880
	global_load_dwordx4 v[28:31], v2, s[62:63] sc1 nt
	global_load_dwordx4 v[60:63], v2, s[62:63] offset:512 sc1 nt
	s_waitcnt vmcnt(31)
	v_cvt_pk_f16_f32 v4, v32, v33
	v_cvt_pk_f16_f32 v5, v34, v35
	ds_write_b64 v141, v[4:5] offset:13056
	s_waitcnt vmcnt(30)
	v_cvt_pk_f16_f32 v4, v64, v65
	v_cvt_pk_f16_f32 v5, v66, v67
	ds_write_b64 v142, v[4:5] offset:13056
	global_load_dwordx4 v[32:35], v2, s[64:65] sc1 nt
	global_load_dwordx4 v[64:67], v2, s[64:65] offset:512 sc1 nt
	s_waitcnt vmcnt(31)
	v_cvt_pk_f16_f32 v4, v36, v37
	v_cvt_pk_f16_f32 v5, v38, v39
	ds_write_b64 v141, v[4:5] offset:15232
	s_waitcnt vmcnt(30)
	v_cvt_pk_f16_f32 v4, v68, v69
	v_cvt_pk_f16_f32 v5, v70, v71
	ds_write_b64 v142, v[4:5] offset:15232
	global_load_dwordx4 v[36:39], v2, s[66:67] sc1 nt
	global_load_dwordx4 v[68:71], v2, s[66:67] offset:512 sc1 nt
	s_waitcnt lgkmcnt(0)
	s_barrier
	s_waitcnt lgkmcnt(0)
	s_barrier
	s_waitcnt vmcnt(31)
	v_cvt_pk_f16_f32 v4, v72, v73
	v_cvt_pk_f16_f32 v5, v74, v75
	ds_write_b64 v143, v[4:5]
	s_waitcnt vmcnt(30)
	v_cvt_pk_f16_f32 v4, v104, v105
	v_cvt_pk_f16_f32 v5, v106, v107
	ds_write_b64 v144, v[4:5]
	global_load_dwordx4 v[72:75], v2, s[52:53] offset:1024 sc1 nt
	global_load_dwordx4 v[104:107], v2, s[52:53] offset:1536 sc1 nt
	s_waitcnt vmcnt(31)
	v_cvt_pk_f16_f32 v4, v76, v77
	v_cvt_pk_f16_f32 v5, v78, v79
	ds_write_b64 v143, v[4:5] offset:2176
	s_waitcnt vmcnt(30)
	v_cvt_pk_f16_f32 v4, v108, v109
	v_cvt_pk_f16_f32 v5, v110, v111
	ds_write_b64 v144, v[4:5] offset:2176
	global_load_dwordx4 v[76:79], v2, s[54:55] offset:1024 sc1 nt
	global_load_dwordx4 v[108:111], v2, s[54:55] offset:1536 sc1 nt
	s_waitcnt vmcnt(31)
	v_cvt_pk_f16_f32 v4, v80, v81
	v_cvt_pk_f16_f32 v5, v82, v83
	ds_write_b64 v143, v[4:5] offset:4352
	s_waitcnt vmcnt(30)
	v_cvt_pk_f16_f32 v4, v112, v113
	v_cvt_pk_f16_f32 v5, v114, v115
	ds_write_b64 v144, v[4:5] offset:4352
	global_load_dwordx4 v[80:83], v2, s[56:57] offset:1024 sc1 nt
	global_load_dwordx4 v[112:115], v2, s[56:57] offset:1536 sc1 nt
	s_waitcnt vmcnt(31)
	v_cvt_pk_f16_f32 v4, v84, v85
	v_cvt_pk_f16_f32 v5, v86, v87
	ds_write_b64 v143, v[4:5] offset:6528
	s_waitcnt vmcnt(30)
	v_cvt_pk_f16_f32 v4, v116, v117
	v_cvt_pk_f16_f32 v5, v118, v119
	ds_write_b64 v144, v[4:5] offset:6528
	global_load_dwordx4 v[84:87], v2, s[58:59] offset:1024 sc1 nt
	global_load_dwordx4 v[116:119], v2, s[58:59] offset:1536 sc1 nt
	s_waitcnt vmcnt(31)
	v_cvt_pk_f16_f32 v4, v88, v89
	v_cvt_pk_f16_f32 v5, v90, v91
	ds_write_b64 v143, v[4:5] offset:8704
	s_waitcnt vmcnt(30)
	v_cvt_pk_f16_f32 v4, v120, v121
	v_cvt_pk_f16_f32 v5, v122, v123
	ds_write_b64 v144, v[4:5] offset:8704
	global_load_dwordx4 v[88:91], v2, s[60:61] offset:1024 sc1 nt
	global_load_dwordx4 v[120:123], v2, s[60:61] offset:1536 sc1 nt
	s_waitcnt vmcnt(31)
	v_cvt_pk_f16_f32 v4, v92, v93
	v_cvt_pk_f16_f32 v5, v94, v95
	ds_write_b64 v143, v[4:5] offset:10880
	s_waitcnt vmcnt(30)
	v_cvt_pk_f16_f32 v4, v124, v125
	v_cvt_pk_f16_f32 v5, v126, v127
	ds_write_b64 v144, v[4:5] offset:10880
	global_load_dwordx4 v[92:95], v2, s[62:63] offset:1024 sc1 nt
	global_load_dwordx4 v[124:127], v2, s[62:63] offset:1536 sc1 nt
	s_waitcnt vmcnt(31)
	v_cvt_pk_f16_f32 v4, v96, v97
	v_cvt_pk_f16_f32 v5, v98, v99
	ds_write_b64 v143, v[4:5] offset:13056
	s_waitcnt vmcnt(30)
	v_cvt_pk_f16_f32 v4, v128, v129
	v_cvt_pk_f16_f32 v5, v130, v131
	ds_write_b64 v144, v[4:5] offset:13056
	global_load_dwordx4 v[96:99], v2, s[64:65] offset:1024 sc1 nt
	global_load_dwordx4 v[128:131], v2, s[64:65] offset:1536 sc1 nt
	s_waitcnt vmcnt(31)
	v_cvt_pk_f16_f32 v4, v100, v101
	v_cvt_pk_f16_f32 v5, v102, v103
	ds_write_b64 v143, v[4:5] offset:15232
	s_waitcnt vmcnt(30)
	v_cvt_pk_f16_f32 v4, v132, v133
	v_cvt_pk_f16_f32 v5, v134, v135
	ds_write_b64 v144, v[4:5] offset:15232
	global_load_dwordx4 v[100:103], v2, s[66:67] offset:1024 sc1 nt
	global_load_dwordx4 v[132:135], v2, s[66:67] offset:1536 sc1 nt
	s_waitcnt lgkmcnt(0)
	s_barrier
	s_waitcnt lgkmcnt(0)
	s_barrier
	s_waitcnt vmcnt(31)
	v_cvt_pk_f16_f32 v4, v8, v9
	v_cvt_pk_f16_f32 v5, v10, v11
	ds_write_b64 v141, v[4:5]
	s_waitcnt vmcnt(30)
	v_cvt_pk_f16_f32 v4, v40, v41
	v_cvt_pk_f16_f32 v5, v42, v43
	ds_write_b64 v142, v[4:5]
	global_load_dwordx4 v[8:11], v2, s[52:53] offset:2048 sc1 nt
	global_load_dwordx4 v[40:43], v2, s[52:53] offset:2560 sc1 nt
	s_waitcnt vmcnt(31)
	v_cvt_pk_f16_f32 v4, v12, v13
	v_cvt_pk_f16_f32 v5, v14, v15
	ds_write_b64 v141, v[4:5] offset:2176
	s_waitcnt vmcnt(30)
	v_cvt_pk_f16_f32 v4, v44, v45
	v_cvt_pk_f16_f32 v5, v46, v47
	ds_write_b64 v142, v[4:5] offset:2176
	global_load_dwordx4 v[12:15], v2, s[54:55] offset:2048 sc1 nt
	global_load_dwordx4 v[44:47], v2, s[54:55] offset:2560 sc1 nt
	s_waitcnt vmcnt(31)
	v_cvt_pk_f16_f32 v4, v16, v17
	v_cvt_pk_f16_f32 v5, v18, v19
	ds_write_b64 v141, v[4:5] offset:4352
	s_waitcnt vmcnt(30)
	v_cvt_pk_f16_f32 v4, v48, v49
	v_cvt_pk_f16_f32 v5, v50, v51
	ds_write_b64 v142, v[4:5] offset:4352
	global_load_dwordx4 v[16:19], v2, s[56:57] offset:2048 sc1 nt
	global_load_dwordx4 v[48:51], v2, s[56:57] offset:2560 sc1 nt
	s_waitcnt vmcnt(31)
	v_cvt_pk_f16_f32 v4, v20, v21
	v_cvt_pk_f16_f32 v5, v22, v23
	ds_write_b64 v141, v[4:5] offset:6528
	s_waitcnt vmcnt(30)
	v_cvt_pk_f16_f32 v4, v52, v53
	v_cvt_pk_f16_f32 v5, v54, v55
	ds_write_b64 v142, v[4:5] offset:6528
	global_load_dwordx4 v[20:23], v2, s[58:59] offset:2048 sc1 nt
	global_load_dwordx4 v[52:55], v2, s[58:59] offset:2560 sc1 nt
	s_waitcnt vmcnt(31)
	v_cvt_pk_f16_f32 v4, v24, v25
	v_cvt_pk_f16_f32 v5, v26, v27
	ds_write_b64 v141, v[4:5] offset:8704
	s_waitcnt vmcnt(30)
	v_cvt_pk_f16_f32 v4, v56, v57
	v_cvt_pk_f16_f32 v5, v58, v59
	ds_write_b64 v142, v[4:5] offset:8704
	global_load_dwordx4 v[24:27], v2, s[60:61] offset:2048 sc1 nt
	global_load_dwordx4 v[56:59], v2, s[60:61] offset:2560 sc1 nt
	s_waitcnt vmcnt(31)
	v_cvt_pk_f16_f32 v4, v28, v29
	v_cvt_pk_f16_f32 v5, v30, v31
	ds_write_b64 v141, v[4:5] offset:10880
	s_waitcnt vmcnt(30)
	v_cvt_pk_f16_f32 v4, v60, v61
	v_cvt_pk_f16_f32 v5, v62, v63
	ds_write_b64 v142, v[4:5] offset:10880
	global_load_dwordx4 v[28:31], v2, s[62:63] offset:2048 sc1 nt
	global_load_dwordx4 v[60:63], v2, s[62:63] offset:2560 sc1 nt
	s_waitcnt vmcnt(31)
	v_cvt_pk_f16_f32 v4, v32, v33
	v_cvt_pk_f16_f32 v5, v34, v35
	ds_write_b64 v141, v[4:5] offset:13056
	s_waitcnt vmcnt(30)
	v_cvt_pk_f16_f32 v4, v64, v65
	v_cvt_pk_f16_f32 v5, v66, v67
	ds_write_b64 v142, v[4:5] offset:13056
	global_load_dwordx4 v[32:35], v2, s[64:65] offset:2048 sc1 nt
	global_load_dwordx4 v[64:67], v2, s[64:65] offset:2560 sc1 nt
	s_waitcnt vmcnt(31)
	v_cvt_pk_f16_f32 v4, v36, v37
	v_cvt_pk_f16_f32 v5, v38, v39
	ds_write_b64 v141, v[4:5] offset:15232
	s_waitcnt vmcnt(30)
	v_cvt_pk_f16_f32 v4, v68, v69
	v_cvt_pk_f16_f32 v5, v70, v71
	ds_write_b64 v142, v[4:5] offset:15232
	global_load_dwordx4 v[36:39], v2, s[66:67] offset:2048 sc1 nt
	global_load_dwordx4 v[68:71], v2, s[66:67] offset:2560 sc1 nt
	s_waitcnt lgkmcnt(0)
	s_barrier
	s_waitcnt lgkmcnt(0)
	s_barrier
	s_waitcnt vmcnt(31)
	v_cvt_pk_f16_f32 v4, v72, v73
	v_cvt_pk_f16_f32 v5, v74, v75
	ds_write_b64 v143, v[4:5]
	s_waitcnt vmcnt(30)
	v_cvt_pk_f16_f32 v4, v104, v105
	v_cvt_pk_f16_f32 v5, v106, v107
	ds_write_b64 v144, v[4:5]
	global_load_dwordx4 v[72:75], v2, s[52:53] offset:3072 sc1 nt
	v_mov_b32_e32 v104, 0
	v_mov_b32_e32 v105, 0
	v_mov_b32_e32 v106, 0
	v_mov_b32_e32 v107, 0
	s_mov_b64 s[70:71], exec
	s_mov_b64 exec, s[68:69]
	global_load_dwordx4 v[104:107], v2, s[52:53] offset:3584 sc1 nt
	s_mov_b64 exec, s[70:71]
	s_waitcnt vmcnt(31)
	v_cvt_pk_f16_f32 v4, v76, v77
	v_cvt_pk_f16_f32 v5, v78, v79
	ds_write_b64 v143, v[4:5] offset:2176
	s_waitcnt vmcnt(30)
	v_cvt_pk_f16_f32 v4, v108, v109
	v_cvt_pk_f16_f32 v5, v110, v111
	ds_write_b64 v144, v[4:5] offset:2176
	global_load_dwordx4 v[76:79], v2, s[54:55] offset:3072 sc1 nt
	v_mov_b32_e32 v108, 0
	v_mov_b32_e32 v109, 0
	v_mov_b32_e32 v110, 0
	v_mov_b32_e32 v111, 0
	s_mov_b64 s[70:71], exec
	s_mov_b64 exec, s[68:69]
	global_load_dwordx4 v[108:111], v2, s[54:55] offset:3584 sc1 nt
	s_mov_b64 exec, s[70:71]
	s_waitcnt vmcnt(31)
	v_cvt_pk_f16_f32 v4, v80, v81
	v_cvt_pk_f16_f32 v5, v82, v83
	ds_write_b64 v143, v[4:5] offset:4352
	s_waitcnt vmcnt(30)
	v_cvt_pk_f16_f32 v4, v112, v113
	v_cvt_pk_f16_f32 v5, v114, v115
	ds_write_b64 v144, v[4:5] offset:4352
	global_load_dwordx4 v[80:83], v2, s[56:57] offset:3072 sc1 nt
	v_mov_b32_e32 v112, 0
	v_mov_b32_e32 v113, 0
	v_mov_b32_e32 v114, 0
	v_mov_b32_e32 v115, 0
	s_mov_b64 s[70:71], exec
	s_mov_b64 exec, s[68:69]
	global_load_dwordx4 v[112:115], v2, s[56:57] offset:3584 sc1 nt
	s_mov_b64 exec, s[70:71]
	s_waitcnt vmcnt(31)
	v_cvt_pk_f16_f32 v4, v84, v85
	v_cvt_pk_f16_f32 v5, v86, v87
	ds_write_b64 v143, v[4:5] offset:6528
	s_waitcnt vmcnt(30)
	v_cvt_pk_f16_f32 v4, v116, v117
	v_cvt_pk_f16_f32 v5, v118, v119
	ds_write_b64 v144, v[4:5] offset:6528
	global_load_dwordx4 v[84:87], v2, s[58:59] offset:3072 sc1 nt
	v_mov_b32_e32 v116, 0
	v_mov_b32_e32 v117, 0
	v_mov_b32_e32 v118, 0
	v_mov_b32_e32 v119, 0
	s_mov_b64 s[70:71], exec
	s_mov_b64 exec, s[68:69]
	global_load_dwordx4 v[116:119], v2, s[58:59] offset:3584 sc1 nt
	s_mov_b64 exec, s[70:71]
	s_waitcnt vmcnt(31)
	v_cvt_pk_f16_f32 v4, v88, v89
	v_cvt_pk_f16_f32 v5, v90, v91
	ds_write_b64 v143, v[4:5] offset:8704
	s_waitcnt vmcnt(30)
	v_cvt_pk_f16_f32 v4, v120, v121
	v_cvt_pk_f16_f32 v5, v122, v123
	ds_write_b64 v144, v[4:5] offset:8704
	global_load_dwordx4 v[88:91], v2, s[60:61] offset:3072 sc1 nt
	v_mov_b32_e32 v120, 0
	v_mov_b32_e32 v121, 0
	v_mov_b32_e32 v122, 0
	v_mov_b32_e32 v123, 0
	s_mov_b64 s[70:71], exec
	s_mov_b64 exec, s[68:69]
	global_load_dwordx4 v[120:123], v2, s[60:61] offset:3584 sc1 nt
	s_mov_b64 exec, s[70:71]
	s_waitcnt vmcnt(31)
	v_cvt_pk_f16_f32 v4, v92, v93
	v_cvt_pk_f16_f32 v5, v94, v95
	ds_write_b64 v143, v[4:5] offset:10880
	s_waitcnt vmcnt(30)
	v_cvt_pk_f16_f32 v4, v124, v125
	v_cvt_pk_f16_f32 v5, v126, v127
	ds_write_b64 v144, v[4:5] offset:10880
	global_load_dwordx4 v[92:95], v2, s[62:63] offset:3072 sc1 nt
	v_mov_b32_e32 v124, 0
	v_mov_b32_e32 v125, 0
	v_mov_b32_e32 v126, 0
	v_mov_b32_e32 v127, 0
	s_mov_b64 s[70:71], exec
	s_mov_b64 exec, s[68:69]
	global_load_dwordx4 v[124:127], v2, s[62:63] offset:3584 sc1 nt
	s_mov_b64 exec, s[70:71]
	s_waitcnt vmcnt(31)
	v_cvt_pk_f16_f32 v4, v96, v97
	v_cvt_pk_f16_f32 v5, v98, v99
	ds_write_b64 v143, v[4:5] offset:13056
	s_waitcnt vmcnt(30)
	v_cvt_pk_f16_f32 v4, v128, v129
	v_cvt_pk_f16_f32 v5, v130, v131
	ds_write_b64 v144, v[4:5] offset:13056
	global_load_dwordx4 v[96:99], v2, s[64:65] offset:3072 sc1 nt
	v_mov_b32_e32 v128, 0
	v_mov_b32_e32 v129, 0
	v_mov_b32_e32 v130, 0
	v_mov_b32_e32 v131, 0
	s_mov_b64 s[70:71], exec
	s_mov_b64 exec, s[68:69]
	global_load_dwordx4 v[128:131], v2, s[64:65] offset:3584 sc1 nt
	s_mov_b64 exec, s[70:71]
	s_waitcnt vmcnt(31)
	v_cvt_pk_f16_f32 v4, v100, v101
	v_cvt_pk_f16_f32 v5, v102, v103
	ds_write_b64 v143, v[4:5] offset:15232
	s_waitcnt vmcnt(30)
	v_cvt_pk_f16_f32 v4, v132, v133
	v_cvt_pk_f16_f32 v5, v134, v135
	ds_write_b64 v144, v[4:5] offset:15232
	global_load_dwordx4 v[100:103], v2, s[66:67] offset:3072 sc1 nt
	v_mov_b32_e32 v132, 0
	v_mov_b32_e32 v133, 0
	v_mov_b32_e32 v134, 0
	v_mov_b32_e32 v135, 0
	s_mov_b64 s[70:71], exec
	s_mov_b64 exec, s[68:69]
	global_load_dwordx4 v[132:135], v2, s[66:67] offset:3584 sc1 nt
	s_mov_b64 exec, s[70:71]
	s_waitcnt lgkmcnt(0)
	s_barrier
	s_waitcnt lgkmcnt(0)
	s_barrier
	s_waitcnt vmcnt(31)
	v_cvt_pk_f16_f32 v4, v8, v9
	v_cvt_pk_f16_f32 v5, v10, v11
	ds_write_b64 v141, v[4:5]
	s_waitcnt vmcnt(30)
	v_cvt_pk_f16_f32 v4, v40, v41
	v_cvt_pk_f16_f32 v5, v42, v43
	ds_write_b64 v142, v[4:5]
	s_waitcnt vmcnt(29)
	v_cvt_pk_f16_f32 v4, v12, v13
	v_cvt_pk_f16_f32 v5, v14, v15
	ds_write_b64 v141, v[4:5] offset:2176
	s_waitcnt vmcnt(28)
	v_cvt_pk_f16_f32 v4, v44, v45
	v_cvt_pk_f16_f32 v5, v46, v47
	ds_write_b64 v142, v[4:5] offset:2176
	s_waitcnt vmcnt(27)
	v_cvt_pk_f16_f32 v4, v16, v17
	v_cvt_pk_f16_f32 v5, v18, v19
	ds_write_b64 v141, v[4:5] offset:4352
	s_waitcnt vmcnt(26)
	v_cvt_pk_f16_f32 v4, v48, v49
	v_cvt_pk_f16_f32 v5, v50, v51
	ds_write_b64 v142, v[4:5] offset:4352
	s_waitcnt vmcnt(25)
	v_cvt_pk_f16_f32 v4, v20, v21
	v_cvt_pk_f16_f32 v5, v22, v23
	ds_write_b64 v141, v[4:5] offset:6528
	s_waitcnt vmcnt(24)
	v_cvt_pk_f16_f32 v4, v52, v53
	v_cvt_pk_f16_f32 v5, v54, v55
	ds_write_b64 v142, v[4:5] offset:6528
	s_waitcnt vmcnt(23)
	v_cvt_pk_f16_f32 v4, v24, v25
	v_cvt_pk_f16_f32 v5, v26, v27
	ds_write_b64 v141, v[4:5] offset:8704
	s_waitcnt vmcnt(22)
	v_cvt_pk_f16_f32 v4, v56, v57
	v_cvt_pk_f16_f32 v5, v58, v59
	ds_write_b64 v142, v[4:5] offset:8704
	s_waitcnt vmcnt(21)
	v_cvt_pk_f16_f32 v4, v28, v29
	v_cvt_pk_f16_f32 v5, v30, v31
	ds_write_b64 v141, v[4:5] offset:10880
	s_waitcnt vmcnt(20)
	v_cvt_pk_f16_f32 v4, v60, v61
	v_cvt_pk_f16_f32 v5, v62, v63
	ds_write_b64 v142, v[4:5] offset:10880
	s_waitcnt vmcnt(19)
	v_cvt_pk_f16_f32 v4, v32, v33
	v_cvt_pk_f16_f32 v5, v34, v35
	ds_write_b64 v141, v[4:5] offset:13056
	s_waitcnt vmcnt(18)
	v_cvt_pk_f16_f32 v4, v64, v65
	v_cvt_pk_f16_f32 v5, v66, v67
	ds_write_b64 v142, v[4:5] offset:13056
	s_waitcnt vmcnt(17)
	v_cvt_pk_f16_f32 v4, v36, v37
	v_cvt_pk_f16_f32 v5, v38, v39
	ds_write_b64 v141, v[4:5] offset:15232
	s_waitcnt vmcnt(16)
	v_cvt_pk_f16_f32 v4, v68, v69
	v_cvt_pk_f16_f32 v5, v70, v71
	ds_write_b64 v142, v[4:5] offset:15232
	s_waitcnt lgkmcnt(0)
	s_barrier
	s_waitcnt lgkmcnt(0)
	s_barrier
	s_waitcnt vmcnt(15)
	v_cvt_pk_f16_f32 v4, v72, v73
	v_cvt_pk_f16_f32 v5, v74, v75
	ds_write_b64 v143, v[4:5]
	s_waitcnt vmcnt(14)
	v_cvt_pk_f16_f32 v4, v104, v105
	v_cvt_pk_f16_f32 v5, v106, v107
	s_mov_b64 s[70:71], exec
	s_mov_b64 exec, s[78:79]
	ds_write_b64 v144, v[4:5]
	s_mov_b64 exec, s[70:71]
	s_waitcnt vmcnt(13)
	v_cvt_pk_f16_f32 v4, v76, v77
	v_cvt_pk_f16_f32 v5, v78, v79
	ds_write_b64 v143, v[4:5] offset:2176
	s_waitcnt vmcnt(12)
	v_cvt_pk_f16_f32 v4, v108, v109
	v_cvt_pk_f16_f32 v5, v110, v111
	s_mov_b64 s[70:71], exec
	s_mov_b64 exec, s[78:79]
	ds_write_b64 v144, v[4:5] offset:2176
	s_mov_b64 exec, s[70:71]
	s_waitcnt vmcnt(11)
	v_cvt_pk_f16_f32 v4, v80, v81
	v_cvt_pk_f16_f32 v5, v82, v83
	ds_write_b64 v143, v[4:5] offset:4352
	s_waitcnt vmcnt(10)
	v_cvt_pk_f16_f32 v4, v112, v113
	v_cvt_pk_f16_f32 v5, v114, v115
	s_mov_b64 s[70:71], exec
	s_mov_b64 exec, s[78:79]
	ds_write_b64 v144, v[4:5] offset:4352
	s_mov_b64 exec, s[70:71]
	s_waitcnt vmcnt(9)
	v_cvt_pk_f16_f32 v4, v84, v85
	v_cvt_pk_f16_f32 v5, v86, v87
	ds_write_b64 v143, v[4:5] offset:6528
	s_waitcnt vmcnt(8)
	v_cvt_pk_f16_f32 v4, v116, v117
	v_cvt_pk_f16_f32 v5, v118, v119
	s_mov_b64 s[70:71], exec
	s_mov_b64 exec, s[78:79]
	ds_write_b64 v144, v[4:5] offset:6528
	s_mov_b64 exec, s[70:71]
	s_waitcnt vmcnt(7)
	v_cvt_pk_f16_f32 v4, v88, v89
	v_cvt_pk_f16_f32 v5, v90, v91
	ds_write_b64 v143, v[4:5] offset:8704
	s_waitcnt vmcnt(6)
	v_cvt_pk_f16_f32 v4, v120, v121
	v_cvt_pk_f16_f32 v5, v122, v123
	s_mov_b64 s[70:71], exec
	s_mov_b64 exec, s[78:79]
	ds_write_b64 v144, v[4:5] offset:8704
	s_mov_b64 exec, s[70:71]
	s_waitcnt vmcnt(5)
	v_cvt_pk_f16_f32 v4, v92, v93
	v_cvt_pk_f16_f32 v5, v94, v95
	ds_write_b64 v143, v[4:5] offset:10880
	s_waitcnt vmcnt(4)
	v_cvt_pk_f16_f32 v4, v124, v125
	v_cvt_pk_f16_f32 v5, v126, v127
	s_mov_b64 s[70:71], exec
	s_mov_b64 exec, s[78:79]
	ds_write_b64 v144, v[4:5] offset:10880
	s_mov_b64 exec, s[70:71]
	s_waitcnt vmcnt(3)
	v_cvt_pk_f16_f32 v4, v96, v97
	v_cvt_pk_f16_f32 v5, v98, v99
	ds_write_b64 v143, v[4:5] offset:13056
	s_waitcnt vmcnt(2)
	v_cvt_pk_f16_f32 v4, v128, v129
	v_cvt_pk_f16_f32 v5, v130, v131
	s_mov_b64 s[70:71], exec
	s_mov_b64 exec, s[78:79]
	ds_write_b64 v144, v[4:5] offset:13056
	s_mov_b64 exec, s[70:71]
	s_waitcnt vmcnt(1)
	v_cvt_pk_f16_f32 v4, v100, v101
	v_cvt_pk_f16_f32 v5, v102, v103
	ds_write_b64 v143, v[4:5] offset:15232
	s_waitcnt vmcnt(0)
	v_cvt_pk_f16_f32 v4, v132, v133
	v_cvt_pk_f16_f32 v5, v134, v135
	s_mov_b64 s[70:71], exec
	s_mov_b64 exec, s[78:79]
	ds_write_b64 v144, v[4:5] offset:15232
	s_mov_b64 exec, s[70:71]
	s_waitcnt lgkmcnt(0)
	s_barrier
	s_waitcnt lgkmcnt(0)
	s_barrier
	s_barrier
	s_barrier
	s_endpgm
